# GEMM1+GEMM2 LDS-DMA pieces reshaped to 8 rows x 128 B full lines with XOR-swizzled row-major LDS image (on top of previous stack)
# speedup vs baseline: 1.0369x; 1.0115x over previous
.LBB0_894:
	s_or_b64 exec, exec, s[2:3]
	v_lshrrev_b32_e32 v0, 3, v3
	v_and_b32_e32 v1, 7, v3
	v_bfe_u32 v4, v0, 1, 3
	v_and_b32_e32 v4, 5, v4
	v_xor_b32_e32 v1, v1, v4
	v_lshlrev_b32_e32 v1, 4, v1
	v_lshrrev_b32_e32 v4, 5, v0
	v_lshlrev_b32_e32 v4, 6, v4
	v_bfe_u32 v5, v0, 2, 2
	v_lshl_or_b32 v4, v5, 4, v4
	v_bfe_u32 v5, v0, 4, 1
	v_lshl_or_b32 v4, v5, 2, v4
	v_and_b32_e32 v5, 3, v0
	v_or_b32_e32 v4, v4, v5
	v_lshl_add_u32 v176, v4, 11, v1
	v_add_u32_e32 v178, 0x40000, v176
	s_waitcnt lgkmcnt(0)
	s_barrier
	v_mbcnt_lo_u32_b32 v0, -1, 0
	v_mbcnt_hi_u32_b32 v0, -1, v0
	s_waitcnt lgkmcnt(0)
	s_add_u32 s12, s10, 0x36000000
	v_add_u32_e32 v0, s33, v0
	v_ashrrev_i32_e32 v3, 31, v0
	v_lshrrev_b32_e32 v3, 26, v3
	v_lshlrev_b32_e32 v1, 4, v0
	v_add_u32_e32 v3, v0, v3
	v_bfe_i32 v0, v0, 27, 1
	v_lshrrev_b32_e32 v0, 22, v0
	v_add_u32_e32 v0, v1, v0
	v_and_b32_e32 v0, 0xfffffc00, v0
	v_sub_u32_e32 v0, v1, v0
	v_lshrrev_b32_e32 v5, 5, v0
	v_bitop3_b32 v0, v5, v0, 16 bitop3:0x6c
	v_ashrrev_i32_e32 v5, 31, v0
	v_lshrrev_b32_e32 v5, 26, v5
	v_add_u32_e32 v5, v0, v5
	v_ashrrev_i32_e32 v6, 6, v5
	v_and_b32_e32 v5, 0xffffffc0, v5
	v_ashrrev_i32_e32 v4, 6, v3
	v_and_b32_e32 v3, 64, v3
	v_sub_u32_e32 v0, v0, v5
	v_add_u32_e32 v1, 0x2000, v1
	v_add_u32_e32 v0, v0, v3
	v_ashrrev_i32_e32 v3, 31, v1
	v_lshrrev_b32_e32 v3, 22, v3
	v_add_u32_e32 v3, v1, v3
	v_ashrrev_i32_e32 v3, 10, v3
	s_addc_u32 s13, s11, 0
	s_lshl_b64 s[2:3], s[6:7], 23
	v_mul_i32_i24_e32 v5, 0x400, v3
	s_add_u32 s2, s0, s2
	v_sub_u32_e32 v1, v1, v5
	s_addc_u32 s3, s1, s3
	s_ashr_i32 s5, s4, 31
	v_lshrrev_b32_e32 v5, 5, v1
	s_lshl_b64 s[0:1], s[4:5], 19
	v_bitop3_b32 v1, v5, v1, 16 bitop3:0x6c
	s_add_u32 s0, s2, s0
	v_ashrrev_i32_e32 v7, 31, v1
	s_addc_u32 s1, s3, s1
	v_lshrrev_b32_e32 v7, 26, v7
	s_add_u32 s36, s0, 0x2000000
	v_readlane_b32 s3, v254, 10
	v_lshlrev_b32_e32 v4, 3, v4
	v_lshlrev_b32_e32 v5, 3, v3
	v_add_u32_e32 v7, v1, v7
	s_addc_u32 s37, s1, 0
	s_lshl_b32 s5, s3, 10
	v_and_b32_e32 v4, 0x3ffffff0, v4
	v_and_b32_e32 v5, 0x3ffffff0, v5
	v_ashrrev_i32_e32 v8, 6, v7
	v_and_b32_e32 v7, 0xffffffc0, v7
	v_add_lshl_u32 v4, v6, v4, 2
	v_add_lshl_u32 v5, v8, v5, 2
	s_add_i32 s50, s5, 0
	v_sub_u32_e32 v1, v1, v7
	v_add_u32_e32 v6, 0x24000, v4
	v_add_u32_e32 v7, 0x24000, v5
	v_add_u32_e32 v4, 0x24200, v4
	v_add_u32_e32 v5, 0x24200, v5
	s_add_i32 m0, s50, 0x10000
	s_lshr_b32 s2, s61, 8
	v_add_u32_e32 v8, s33, v2
	v_lshrrev_b32_e32 v6, 3, v8
	v_and_b32_e32 v0, 7, v2
	v_bfe_u32 v1, v6, 1, 3
	v_and_b32_e32 v1, 5, v1
	v_xor_b32_e32 v0, v0, v1
	v_lshlrev_b32_e32 v0, 4, v0
	v_mov_b32_e32 v1, v0
	v_lshlrev_b32_e32 v6, 2, v6
	v_add_u32_e32 v7, 0x24100, v6
	v_add_u32_e32 v4, 0x24200, v6
	v_add_u32_e32 v5, 0x24300, v6
	v_add_u32_e32 v6, 0x24000, v6
	ds_read_b32 v6, v6
	ds_read_b32 v7, v7
	ds_read_b32 v4, v4
	ds_read_b32 v5, v5
	global_load_lds_dwordx4 v176, s[36:37]
	s_add_i32 m0, s50, 0x12000
	s_add_u32 s0, s0, 0x2004000
	s_addc_u32 s1, s1, 0
	global_load_lds_dwordx4 v178, s[36:37]
	s_add_i32 m0, s50, 0x14000
	global_load_lds_dwordx4 v176, s[0:1]
	s_add_i32 m0, s50, 0x16000
	s_waitcnt lgkmcnt(0)
	v_add_u32_e32 v180, v0, v6
	s_add_i32 s51, s50, 0x2000
	global_load_lds_dwordx4 v178, s[0:1]
	s_mov_b32 m0, s50
	v_add_u32_e32 v182, v1, v7
	s_add_i32 s52, s50, 0x4000
	global_load_lds_dwordx4 v180, s[12:13]
	s_mov_b32 m0, s51
	v_add_u32_e32 v0, v0, v4
	s_add_i32 s53, s50, 0x6000
	global_load_lds_dwordx4 v182, s[12:13]
	s_mov_b32 m0, s52
	v_add_u32_e32 v186, v1, v5
	s_cmp_eq_u32 s2, 1
	global_load_lds_dwordx4 v0, s[12:13]
	s_mov_b32 m0, s53
	s_movk_i32 s54, 0x2000
	global_load_lds_dwordx4 v186, s[12:13]
	s_mov_b32 s55, 0
	s_movk_i32 s56, 0x4000
	s_cselect_b64 s[0:1], -1, 0
	s_cmp_lg_u32 s2, 1
	s_movk_i32 s57, 0x6000
	s_cbranch_scc1 .LBB0_896
	s_barrier
.LBB0_896:
	v_readlane_b32 s3, v254, 10
	s_lshl_b32 s59, s2, 6
	v_ashrrev_i32_e32 v4, 5, v2
	s_lshl_b32 s2, s2, 13
	v_lshlrev_b32_e32 v1, 1, v2
	v_lshl_add_u32 v5, v4, 10, s2
	s_lshl_b32 s2, s3, 5
	v_and_b32_e32 v3, 32, v1
	v_lshlrev_b32_e32 v2, 6, v2
	s_and_b32 s60, s2, 0x60
	v_or_b32_e32 v6, v5, v3
	v_and_b32_e32 v2, 0x3c0, v2
	v_and_b32_e32 v1, 16, v1
	s_lshr_b32 s2, s60, 3
	v_or3_b32 v6, v6, v2, v1
	v_add_lshl_u32 v4, v4, s2, 10
	v_or_b32_e32 v2, v2, v3
	v_or3_b32 v194, v2, v4, v1
	v_or_b32_e32 v2, 16, v2
	v_mov_b32_e32 v177, 0
	v_bitop3_b32 v5, v2, v5, v1 bitop3:0xde
	v_bitop3_b32 v195, v2, v4, v1 bitop3:0xde
	v_mbcnt_lo_u32_b32 v1, -1, 0
	v_mbcnt_hi_u32_b32 v1, -1, v1
	v_and_b32_e32 v4, 15, v1
	v_lshrrev_b32_e32 v1, 4, v1
	v_lshlrev_b32_e32 v1, 1, v1
	v_bfe_u32 v194, v4, 1, 3
	v_and_b32_e32 v194, 5, v194
	v_xor_b32_e32 v1, v1, v194
	v_lshlrev_b32_e32 v1, 4, v1
	v_lshl_add_u32 v1, v4, 7, v1
	v_lshl_add_u32 v6, s59, 7, v1
	v_xor_b32_e32 v5, 16, v6
	v_lshl_add_u32 v194, s60, 7, v1
	v_xor_b32_e32 v195, 16, v194
	s_waitcnt vmcnt(2)
	s_barrier
	s_mov_b64 s[14:15], 0x80
	v_lshl_add_u64 v[2:3], s[36:37], 0, v[176:177]
	s_add_i32 m0, s50, 0x18000
	v_lshl_add_u64 v[2:3], v[2:3], 0, s[14:15]
	s_add_i32 s58, s3, s49
	global_load_lds_dwordx4 v[2:3], off
	v_mov_b32_e32 v179, v177
	s_add_i32 m0, s50, 0x1a000
	s_add_u32 s2, s10, 0x36000080
	v_lshl_add_u64 v[2:3], s[36:37], 0, v[178:179]
	v_lshl_add_u64 v[2:3], v[2:3], 0, s[14:15]
	s_addc_u32 s3, s11, 0
	s_add_i32 s62, s50, 0x8000
	global_load_lds_dwordx4 v[2:3], off
	s_mov_b32 m0, s62
	s_add_i32 s63, s50, 0xa000
	s_mov_b64 s[16:17], 0x36000080
	global_load_lds_dwordx4 v180, s[2:3]
	s_mov_b32 m0, s63
	s_mov_b32 s61, 0x8000
	global_load_lds_dwordx4 v182, s[2:3]
	s_add_u32 s2, s36, 0x4080
	s_addc_u32 s3, s37, 0
	s_add_i32 m0, s50, 0x1c000
	s_movk_i32 s64, 0x100
	global_load_lds_dwordx4 v176, s[2:3]
	s_add_i32 m0, s50, 0x1e000
	v_mov_b32_e32 v184, v176
	global_load_lds_dwordx4 v178, s[2:3]
	s_waitcnt vmcnt(6)
	v_readlane_b32 s2, v254, 15
	s_cmpk_lt_u32 s2, 0x100
	s_cselect_b64 s[18:19], -1, 0
	s_add_i32 s65, s45, -1
	v_mov_b32_e32 v231, 0x24854
	v_mov_b32_e32 v252, 0x24858
	v_mov_b32_e32 v253, 0x2485c
	v_mov_b32_e32 v220, 0x24864
	v_mov_b32_e32 v221, 0x24868
	v_mov_b32_e32 v222, 0x2486c
	v_mov_b32_e32 v223, 0x24870
	v_mov_b32_e32 v224, 0x24874
	v_mov_b32_e32 v225, 0x24878
	v_mov_b32_e32 v226, 0x2487c
	s_mov_b32 s66, 0x25800
	s_add_i32 s67, 0, 0x10000
	s_add_i32 s68, 0, 0x14000
	v_add_u32_e32 v227, 0, v6
	v_add_u32_e32 v228, 0, v5
	v_mov_b32_e32 v229, 0x7f7f7f7f
	s_mov_b64 s[20:21], 0x5e000000
	s_mov_b32 s69, 0xc0c00000
	s_mov_b64 s[22:23], 0x22000000
	s_mov_b32 s70, 0x22001000
	v_mov_b32_e32 v230, 0x41000000
	v_mov_b32_e32 v176, v0
	s_mov_b32 s74, 0
	v_mov_b32_e32 v0, v177
	v_mov_b32_e32 v1, v177
	v_mov_b32_e32 v2, v177
	v_mov_b32_e32 v3, v177
	v_mov_b32_e32 v4, v177
	v_mov_b32_e32 v5, v177
	v_mov_b32_e32 v6, v177
	v_mov_b32_e32 v7, v177
	v_mov_b32_e32 v8, v177
	v_mov_b32_e32 v9, v177
	v_mov_b32_e32 v10, v177
	v_mov_b32_e32 v11, v177
	v_mov_b32_e32 v12, v177
	v_mov_b32_e32 v13, v177
	v_mov_b32_e32 v14, v177
	v_mov_b32_e32 v15, v177
	v_mov_b32_e32 v16, v177
	v_mov_b32_e32 v17, v177
	v_mov_b32_e32 v18, v177
	v_mov_b32_e32 v19, v177
	v_mov_b32_e32 v20, v177
	v_mov_b32_e32 v21, v177
	v_mov_b32_e32 v22, v177
	v_mov_b32_e32 v23, v177
	v_mov_b32_e32 v24, v177
	v_mov_b32_e32 v25, v177
	v_mov_b32_e32 v26, v177
	v_mov_b32_e32 v27, v177
	v_mov_b32_e32 v28, v177
	v_mov_b32_e32 v29, v177
	v_mov_b32_e32 v30, v177
	v_mov_b32_e32 v31, v177
	v_mov_b32_e32 v36, v177
	v_mov_b32_e32 v37, v177
	v_mov_b32_e32 v38, v177
	v_mov_b32_e32 v39, v177
	v_mov_b32_e32 v44, v177
	v_mov_b32_e32 v45, v177
	v_mov_b32_e32 v46, v177
	v_mov_b32_e32 v47, v177
	v_mov_b32_e32 v32, v177
	v_mov_b32_e32 v33, v177
	v_mov_b32_e32 v34, v177
	v_mov_b32_e32 v35, v177
	v_mov_b32_e32 v40, v177
	v_mov_b32_e32 v41, v177
	v_mov_b32_e32 v42, v177
	v_mov_b32_e32 v43, v177
	v_mov_b32_e32 v48, v177
	v_mov_b32_e32 v49, v177
	v_mov_b32_e32 v50, v177
	v_mov_b32_e32 v51, v177
	v_mov_b32_e32 v52, v177
	v_mov_b32_e32 v53, v177
	v_mov_b32_e32 v54, v177
	v_mov_b32_e32 v55, v177
	v_mov_b32_e32 v56, v177
	v_mov_b32_e32 v57, v177
	v_mov_b32_e32 v58, v177
	v_mov_b32_e32 v59, v177
	v_mov_b32_e32 v60, v177
	v_mov_b32_e32 v61, v177
	v_mov_b32_e32 v62, v177
	v_mov_b32_e32 v63, v177
	v_mov_b32_e32 v64, v177
	v_mov_b32_e32 v65, v177
	v_mov_b32_e32 v66, v177
	v_mov_b32_e32 v67, v177
	v_mov_b32_e32 v68, v177
	v_mov_b32_e32 v69, v177
	v_mov_b32_e32 v70, v177
	v_mov_b32_e32 v71, v177
	v_mov_b32_e32 v72, v177
	v_mov_b32_e32 v73, v177
	v_mov_b32_e32 v74, v177
	v_mov_b32_e32 v75, v177
	v_mov_b32_e32 v76, v177
	v_mov_b32_e32 v77, v177
	v_mov_b32_e32 v78, v177
	v_mov_b32_e32 v79, v177
	v_mov_b32_e32 v80, v177
	v_mov_b32_e32 v81, v177
	v_mov_b32_e32 v82, v177
	v_mov_b32_e32 v83, v177
	v_mov_b32_e32 v84, v177
	v_mov_b32_e32 v85, v177
	v_mov_b32_e32 v86, v177
	v_mov_b32_e32 v87, v177
	v_mov_b32_e32 v88, v177
	v_mov_b32_e32 v89, v177
	v_mov_b32_e32 v90, v177
	v_mov_b32_e32 v91, v177
	v_mov_b32_e32 v92, v177
	v_mov_b32_e32 v93, v177
	v_mov_b32_e32 v94, v177
	v_mov_b32_e32 v95, v177
	v_mov_b32_e32 v96, v177
	v_mov_b32_e32 v97, v177
	v_mov_b32_e32 v98, v177
	v_mov_b32_e32 v99, v177
	v_mov_b32_e32 v100, v177
	v_mov_b32_e32 v101, v177
	v_mov_b32_e32 v102, v177
	v_mov_b32_e32 v103, v177
	v_mov_b32_e32 v104, v177
	v_mov_b32_e32 v105, v177
	v_mov_b32_e32 v106, v177
	v_mov_b32_e32 v107, v177
	v_mov_b32_e32 v108, v177
	v_mov_b32_e32 v109, v177
	v_mov_b32_e32 v110, v177
	v_mov_b32_e32 v111, v177
	v_mov_b32_e32 v112, v177
	v_mov_b32_e32 v113, v177
	v_mov_b32_e32 v114, v177
	v_mov_b32_e32 v115, v177
	v_mov_b32_e32 v116, v177
	v_mov_b32_e32 v117, v177
	v_mov_b32_e32 v118, v177
	v_mov_b32_e32 v119, v177
	v_mov_b32_e32 v120, v177
	v_mov_b32_e32 v121, v177
	v_mov_b32_e32 v122, v177
	v_mov_b32_e32 v123, v177
	v_mov_b32_e32 v124, v177
	v_mov_b32_e32 v125, v177
	v_mov_b32_e32 v126, v177
	v_mov_b32_e32 v127, v177
	s_barrier

.LBB0_912:
	s_cmp_eq_u32 s42, 12
	s_cselect_b64 s[40:41], -1, 0
	s_and_b64 s[38:39], s[34:35], s[40:41]
	s_andn2_b64 vcc, exec, s[38:39]
	v_mov_b32_e32 v128, v186
	v_mov_b32_e32 v129, v176
	s_cbranch_vccnz .LBB0_911
	v_mbcnt_lo_u32_b32 v128, -1, 0
	v_mbcnt_hi_u32_b32 v128, -1, v128
	v_and_b32_e32 v132, 7, v128
	v_add_u32_e32 v128, s33, v128
	v_lshrrev_b32_e32 v128, 3, v128
	v_bfe_u32 v133, v128, 1, 3
	v_and_b32_e32 v133, 5, v133
	v_xor_b32_e32 v132, v132, v133
	v_lshlrev_b32_e32 v132, 4, v132
	v_lshl_add_u32 v128, v128, 2, s7
	v_add_u32_e32 v130, 0x100, v128
	ds_read2st64_b32 v[128:129], v128 offset1:2
	ds_read2st64_b32 v[130:131], v130 offset1:2
	s_waitcnt lgkmcnt(0)
	v_add_u32_e32 v180, v132, v128
	v_add_u32_e32 v182, v132, v130
	v_add_u32_e32 v129, v132, v129
	v_add_u32_e32 v128, v132, v131
	s_branch .LBB0_911

.LBB0_993:
	v_add_u32_e32 v1, s33, v0
	v_lshrrev_b32_e32 v2, 3, v1
	v_and_b32_e32 v1, 7, v1
	v_bfe_u32 v4, v2, 1, 3
	v_and_b32_e32 v4, 5, v4
	v_xor_b32_e32 v1, v1, v4
	v_lshlrev_b32_e32 v1, 4, v1
	v_lshrrev_b32_e32 v4, 5, v2
	v_lshlrev_b32_e32 v4, 6, v4
	v_bfe_u32 v5, v2, 2, 2
	v_lshl_or_b32 v4, v5, 4, v4
	v_bfe_u32 v5, v2, 4, 1
	v_lshl_or_b32 v4, v5, 2, v4
	v_and_b32_e32 v5, 3, v2
	v_or_b32_e32 v4, v4, v5
	v_lshl_add_u32 v128, v4, 11, v1
	v_add_u32_e32 v130, 0x40000, v128
	s_waitcnt lgkmcnt(0)
	s_barrier
	v_mbcnt_lo_u32_b32 v1, -1, 0
	v_mbcnt_hi_u32_b32 v1, -1, v1
	s_waitcnt lgkmcnt(0)
	s_add_u32 s10, s6, 0x5e000000
	v_add_u32_e32 v1, s33, v1
	v_ashrrev_i32_e32 v3, 31, v1
	v_lshrrev_b32_e32 v3, 26, v3
	v_lshlrev_b32_e32 v2, 4, v1
	v_add_u32_e32 v3, v1, v3
	v_bfe_i32 v1, v1, 27, 1
	v_lshrrev_b32_e32 v1, 22, v1
	v_add_u32_e32 v1, v2, v1
	v_and_b32_e32 v1, 0xfffffc00, v1
	v_sub_u32_e32 v1, v2, v1
	v_lshrrev_b32_e32 v5, 5, v1
	v_bitop3_b32 v1, v5, v1, 16 bitop3:0x6c
	v_ashrrev_i32_e32 v5, 31, v1
	v_lshrrev_b32_e32 v5, 26, v5
	v_add_u32_e32 v5, v1, v5
	v_ashrrev_i32_e32 v6, 6, v5
	v_and_b32_e32 v5, 0xffffffc0, v5
	v_ashrrev_i32_e32 v4, 6, v3
	v_and_b32_e32 v3, 64, v3
	v_sub_u32_e32 v1, v1, v5
	v_add_u32_e32 v2, 0x2000, v2
	v_add_u32_e32 v1, v1, v3
	v_ashrrev_i32_e32 v3, 31, v2
	v_lshrrev_b32_e32 v3, 22, v3
	v_add_u32_e32 v3, v2, v3
	v_ashrrev_i32_e32 v3, 10, v3
	v_mul_i32_i24_e32 v5, 0x400, v3
	v_sub_u32_e32 v2, v2, v5
	s_addc_u32 s11, s7, 0
	s_lshl_b64 s[12:13], s[4:5], 22
	v_lshlrev_b32_e32 v4, 3, v4
	v_lshrrev_b32_e32 v5, 5, v2
	s_add_u32 s5, s2, s12
	v_and_b32_e32 v4, -16, v4
	v_bitop3_b32 v2, v5, v2, 16 bitop3:0x6c
	s_addc_u32 s12, s3, s13
	s_ashr_i32 s1, s0, 31
	v_add_u32_e32 v4, v6, v4
	v_ashrrev_i32_e32 v6, 31, v2
	s_lshl_b64 s[2:3], s[0:1], 19
	v_lshrrev_b32_e32 v6, 26, v6
	s_add_u32 s5, s5, s2
	v_add_u32_e32 v6, v2, v6
	s_addc_u32 s3, s12, s3
	v_lshlrev_b32_e32 v5, 3, v3
	v_ashrrev_i32_e32 v7, 6, v6
	v_lshlrev_b32_e32 v3, 6, v3
	v_and_b32_e32 v6, 0xffffffc0, v6
	s_add_u32 s38, s5, 0x22000000
	v_and_b32_e32 v5, -16, v5
	v_and_b32_e32 v3, 64, v3
	v_sub_u32_e32 v2, v2, v6
	s_addc_u32 s39, s3, 0
	v_add_u32_e32 v5, v7, v5
	v_add_u32_e32 v2, v2, v3
	v_add_u32_e32 v6, s33, v0
	v_lshrrev_b32_e32 v4, 3, v6
	v_add_u32_e32 v5, 64, v4
	v_and_b32_e32 v1, 7, v0
	v_bfe_u32 v6, v4, 1, 3
	v_and_b32_e32 v6, 5, v6
	v_xor_b32_e32 v1, v1, v6
	v_lshlrev_b32_e32 v1, 4, v1
	v_mov_b32_e32 v2, v1
	s_lshl_b32 s1, s16, 19
	v_lshlrev_b32_e32 v3, 11, v4
	v_add3_u32 v132, v1, s1, v3
	v_lshlrev_b32_e32 v3, 11, v5
	v_add3_u32 v134, v2, s1, v3
	s_lshl_b32 s1, s16, 8
	s_bitset1_b32 s1, 7
	v_add_u32_e32 v3, s1, v4
	v_lshl_add_u32 v1, v3, 11, v1
	v_add_u32_e32 v3, s1, v5
	s_add_i32 s1, s48, 0
	s_add_i32 m0, s1, 0x10000
	s_lshr_b32 s2, s61, 8
	v_lshl_add_u32 v138, v3, 11, v2
	global_load_lds_dwordx4 v128, s[38:39]
	s_add_i32 m0, s1, 0x12000
	s_add_u32 s12, s5, 0x22004000
	s_addc_u32 s13, s3, 0
	global_load_lds_dwordx4 v130, s[38:39]
	s_add_i32 m0, s1, 0x14000
	s_add_i32 s49, s1, 0x2000
	global_load_lds_dwordx4 v128, s[12:13]
	s_add_i32 m0, s1, 0x16000
	s_add_i32 s50, s1, 0x4000
	global_load_lds_dwordx4 v130, s[12:13]
	s_mov_b32 m0, s1
	s_add_i32 s51, s1, 0x6000
	global_load_lds_dwordx4 v132, s[10:11]
	s_mov_b32 m0, s49
	s_cmp_eq_u32 s2, 1
	global_load_lds_dwordx4 v134, s[10:11]
	s_mov_b32 m0, s50
	s_cselect_b64 s[12:13], -1, 0
	global_load_lds_dwordx4 v1, s[10:11]
	s_mov_b32 m0, s51
	s_cmp_lg_u32 s2, 1
	global_load_lds_dwordx4 v138, s[10:11]
	s_mov_b32 s60, 0
	s_cbranch_scc1 .LBB0_995
	s_barrier
.LBB0_995:
	v_lshlrev_b32_e32 v4, 5, v0
	v_lshlrev_b32_e32 v2, 1, v0
	v_and_b32_e32 v4, 0xfffffc00, v4
	v_and_b32_e32 v3, 32, v2
	v_lshl_add_u32 v5, s2, 13, v4
	v_lshlrev_b32_e32 v0, 6, v0
	s_bfe_u32 s5, s61, 0x20006
	v_or_b32_e32 v6, v5, v3
	v_and_b32_e32 v0, 0x3c0, v0
	v_and_b32_e32 v2, 16, v2
	v_or3_b32 v6, v6, v0, v2
	v_lshl_add_u32 v4, s5, 12, v4
	v_or_b32_e32 v0, v0, v3
	v_or3_b32 v142, v0, v4, v2
	v_or_b32_e32 v0, 16, v0
	v_mov_b32_e32 v129, 0
	v_bitop3_b32 v5, v0, v5, v2 bitop3:0xde
	v_bitop3_b32 v143, v0, v4, v2 bitop3:0xde
	v_mbcnt_lo_u32_b32 v0, -1, 0
	v_mbcnt_hi_u32_b32 v0, -1, v0
	v_and_b32_e32 v4, 15, v0
	v_lshrrev_b32_e32 v0, 4, v0
	v_lshlrev_b32_e32 v0, 1, v0
	v_bfe_u32 v2, v4, 1, 3
	v_and_b32_e32 v2, 5, v2
	v_xor_b32_e32 v0, v0, v2
	v_lshlrev_b32_e32 v0, 4, v0
	v_lshl_add_u32 v0, v4, 7, v0
	v_lshl_add_u32 v6, s2, 13, v0
	v_xor_b32_e32 v5, 16, v6
	v_lshl_add_u32 v142, s5, 12, v0
	v_xor_b32_e32 v143, 16, v142
	s_waitcnt vmcnt(2)
	s_barrier
	s_mov_b64 s[14:15], 0x80
	v_lshl_add_u64 v[2:3], s[38:39], 0, v[128:129]
	s_add_i32 m0, s1, 0x18000
	v_lshl_add_u64 v[2:3], v[2:3], 0, s[14:15]
	s_lshl_b32 s52, s2, 6
	global_load_lds_dwordx4 v[2:3], off
	v_mov_b32_e32 v131, v129
	s_add_i32 m0, s1, 0x1a000
	s_add_u32 s2, s6, 0x5e000080
	v_lshl_add_u64 v[2:3], s[38:39], 0, v[130:131]
	v_lshl_add_u64 v[2:3], v[2:3], 0, s[14:15]
	s_addc_u32 s3, s7, 0
	s_add_i32 s53, s1, 0x8000
	global_load_lds_dwordx4 v[2:3], off
	s_mov_b32 m0, s53
	s_add_i32 s54, s1, 0xa000
	s_mov_b64 s[16:17], 0x5e000080
	global_load_lds_dwordx4 v132, s[2:3]
	s_mov_b32 m0, s54
	v_mov_b32_e32 v164, 0x24854
	global_load_lds_dwordx4 v134, s[2:3]
	s_add_u32 s2, s38, 0x4080
	s_addc_u32 s3, s39, 0
	s_add_i32 m0, s1, 0x1c000
	v_mov_b32_e32 v165, 0x24858
	global_load_lds_dwordx4 v128, s[2:3]
	s_add_i32 m0, s1, 0x1e000
	s_cmp_gt_u32 s61, 63
	global_load_lds_dwordx4 v130, s[2:3]
	v_readlane_b32 s2, v254, 10
	s_waitcnt vmcnt(6)
	s_cselect_b64 s[18:19], -1, 0
	s_cmp_eq_u32 s2, 1
	s_mov_b32 s2, 0x1a00000
	s_cselect_b32 s55, s2, 0x12000000
	s_cmpk_lt_u32 s61, 0x100
	v_mov_b32_e32 v136, v128
	s_cselect_b64 s[20:21], -1, 0
	s_lshl_b32 s56, s5, 6
	v_mov_b32_e32 v166, 0x2485c
	v_mov_b32_e32 v167, 0x24860
	v_mov_b32_e32 v168, 0x24864
	v_mov_b32_e32 v169, 0x24868
	v_mov_b32_e32 v170, 0x2486c
	v_mov_b32_e32 v171, 0x24870
	v_mov_b32_e32 v172, 0x24874
	v_mov_b32_e32 v173, 0x24878
	v_mov_b32_e32 v174, 0x2487c
	s_mov_b32 s57, 0x25800
	s_add_i32 s58, 0, 0x10000
	s_add_i32 s59, 0, 0x14000
	v_add_u32_e32 v175, 0, v6
	v_add_u32_e32 v176, 0, v5
	v_mov_b32_e32 v177, 0x7f7f7f7f
	s_mov_b64 s[22:23], 0x80000000
	s_mov_b32 s24, 0x3b800000
	v_mov_b32_e32 v128, v1
	v_mov_b32_e32 v0, v129
	v_mov_b32_e32 v1, v129
	v_mov_b32_e32 v2, v129
	v_mov_b32_e32 v3, v129
	v_mov_b32_e32 v4, v129
	v_mov_b32_e32 v5, v129
	v_mov_b32_e32 v6, v129
	v_mov_b32_e32 v7, v129
	v_mov_b32_e32 v8, v129
	v_mov_b32_e32 v9, v129
	v_mov_b32_e32 v10, v129
	v_mov_b32_e32 v11, v129
	v_mov_b32_e32 v12, v129
	v_mov_b32_e32 v13, v129
	v_mov_b32_e32 v14, v129
	v_mov_b32_e32 v15, v129
	v_mov_b32_e32 v16, v129
	v_mov_b32_e32 v17, v129
	v_mov_b32_e32 v18, v129
	v_mov_b32_e32 v19, v129
	v_mov_b32_e32 v20, v129
	v_mov_b32_e32 v21, v129
	v_mov_b32_e32 v22, v129
	v_mov_b32_e32 v23, v129
	v_mov_b32_e32 v24, v129
	v_mov_b32_e32 v25, v129
	v_mov_b32_e32 v26, v129
	v_mov_b32_e32 v27, v129
	v_mov_b32_e32 v28, v129
	v_mov_b32_e32 v29, v129
	v_mov_b32_e32 v30, v129
	v_mov_b32_e32 v31, v129
	v_mov_b32_e32 v36, v129
	v_mov_b32_e32 v37, v129
	v_mov_b32_e32 v38, v129
	v_mov_b32_e32 v39, v129
	v_mov_b32_e32 v44, v129
	v_mov_b32_e32 v45, v129
	v_mov_b32_e32 v46, v129
	v_mov_b32_e32 v47, v129
	v_mov_b32_e32 v32, v129
	v_mov_b32_e32 v33, v129
	v_mov_b32_e32 v34, v129
	v_mov_b32_e32 v35, v129
	v_mov_b32_e32 v40, v129
	v_mov_b32_e32 v41, v129
	v_mov_b32_e32 v42, v129
	v_mov_b32_e32 v43, v129
	v_mov_b32_e32 v48, v129
	v_mov_b32_e32 v49, v129
	v_mov_b32_e32 v50, v129
	v_mov_b32_e32 v51, v129
	v_mov_b32_e32 v52, v129
	v_mov_b32_e32 v53, v129
	v_mov_b32_e32 v54, v129
	v_mov_b32_e32 v55, v129
	v_mov_b32_e32 v56, v129
	v_mov_b32_e32 v57, v129
	v_mov_b32_e32 v58, v129
	v_mov_b32_e32 v59, v129
	v_mov_b32_e32 v60, v129
	v_mov_b32_e32 v61, v129
	v_mov_b32_e32 v62, v129
	v_mov_b32_e32 v63, v129
	v_mov_b32_e32 v64, v129
	v_mov_b32_e32 v65, v129
	v_mov_b32_e32 v66, v129
	v_mov_b32_e32 v67, v129
	v_mov_b32_e32 v68, v129
	v_mov_b32_e32 v69, v129
	v_mov_b32_e32 v70, v129
	v_mov_b32_e32 v71, v129
	v_mov_b32_e32 v72, v129
	v_mov_b32_e32 v73, v129
	v_mov_b32_e32 v74, v129
	v_mov_b32_e32 v75, v129
	v_mov_b32_e32 v76, v129
	v_mov_b32_e32 v77, v129
	v_mov_b32_e32 v78, v129
	v_mov_b32_e32 v79, v129
	v_mov_b32_e32 v80, v129
	v_mov_b32_e32 v81, v129
	v_mov_b32_e32 v82, v129
	v_mov_b32_e32 v83, v129
	v_mov_b32_e32 v84, v129
	v_mov_b32_e32 v85, v129
	v_mov_b32_e32 v86, v129
	v_mov_b32_e32 v87, v129
	v_mov_b32_e32 v88, v129
	v_mov_b32_e32 v89, v129
	v_mov_b32_e32 v90, v129
	v_mov_b32_e32 v91, v129
	v_mov_b32_e32 v92, v129
	v_mov_b32_e32 v93, v129
	v_mov_b32_e32 v94, v129
	v_mov_b32_e32 v95, v129
	v_mov_b32_e32 v96, v129
	v_mov_b32_e32 v97, v129
	v_mov_b32_e32 v98, v129
	v_mov_b32_e32 v99, v129
	v_mov_b32_e32 v100, v129
	v_mov_b32_e32 v101, v129
	v_mov_b32_e32 v102, v129
	v_mov_b32_e32 v103, v129
	v_mov_b32_e32 v104, v129
	v_mov_b32_e32 v105, v129
	v_mov_b32_e32 v106, v129
	v_mov_b32_e32 v107, v129
	v_mov_b32_e32 v108, v129
	v_mov_b32_e32 v109, v129
	v_mov_b32_e32 v110, v129
	v_mov_b32_e32 v111, v129
	v_mov_b32_e32 v112, v129
	v_mov_b32_e32 v113, v129
	v_mov_b32_e32 v114, v129
	v_mov_b32_e32 v115, v129
	v_mov_b32_e32 v116, v129
	v_mov_b32_e32 v117, v129
	v_mov_b32_e32 v118, v129
	v_mov_b32_e32 v119, v129
	v_mov_b32_e32 v120, v129
	v_mov_b32_e32 v121, v129
	v_mov_b32_e32 v122, v129
	v_mov_b32_e32 v123, v129
	v_mov_b32_e32 v124, v129
	v_mov_b32_e32 v125, v129
	v_mov_b32_e32 v126, v129
	v_mov_b32_e32 v127, v129
	s_barrier
	s_branch .LBB0_997

.LBB0_1010:
	s_cmp_eq_u32 s45, 12
	s_cselect_b64 s[42:43], -1, 0
	s_and_b64 s[40:41], s[36:37], s[42:43]
	s_andn2_b64 vcc, exec, s[40:41]
	v_mov_b32_e32 v131, v138
	v_mov_b32_e32 v133, v128
	s_cbranch_vccnz .LBB0_1009
	v_mbcnt_lo_u32_b32 v131, -1, 0
	v_mbcnt_hi_u32_b32 v131, -1, v131
	v_and_b32_e32 v135, 7, v131
	v_add_u32_e32 v131, s33, v131
	v_lshrrev_b32_e32 v137, 3, v131
	v_bfe_u32 v131, v137, 1, 3
	v_and_b32_e32 v131, 5, v131
	v_xor_b32_e32 v135, v135, v131
	v_lshlrev_b32_e32 v135, 4, v135
	v_add_u32_e32 v139, 64, v137
	v_lshlrev_b32_e32 v133, 11, v139
	v_lshlrev_b32_e32 v132, 11, v137
	v_add3_u32 v134, v135, s29, v133
	v_add_u32_e32 v133, s44, v137
	v_add3_u32 v132, v135, s29, v132
	v_lshl_add_u32 v133, v133, 11, v135
	v_add_u32_e32 v131, s44, v139
	v_lshl_add_u32 v131, v131, 11, v135
	s_branch .LBB0_1009
